# attention-A: two-slot K/V LDS rings with static immediate offsets (drops per-tile address adds and ring rotation), prologue/epilogue adapted
# speedup vs baseline: 1.0738x; 1.0035x over previous
.LBB0_411:
	s_and_b64 s[62:63], s[28:29], s[4:5]
	s_mul_hi_i32 s5, s56, s46
	s_mul_i32 s4, s56, s46
	s_xor_b64 s[60:61], s[62:63], -1
	s_ashr_i32 s47, s46, 31
	s_lshl_b64 s[4:5], s[4:5], 2
	s_waitcnt lgkmcnt(0)
	s_add_u32 s1, s14, s4
	s_addc_u32 s8, s15, s5
	s_ashr_i32 s11, s10, 31
	s_lshl_b64 s[4:5], s[10:11], 2
	s_add_u32 s58, s1, s4
	s_addc_u32 s59, s8, s5
	s_lshl_b32 s1, s26, 3
	s_add_i32 s4, s1, s33
	s_ashr_i32 s5, s4, 31
	s_ashr_i32 s31, s30, 31
	s_lshl_b64 s[4:5], s[4:5], 21
	s_lshl_b64 s[10:11], s[30:31], 15
	s_add_u32 s1, s73, s4
	s_addc_u32 s4, s75, s5
	v_mbcnt_lo_u32_b32 v9, -1, 0
	v_mbcnt_hi_u32_b32 v9, -1, v9
	v_readlane_b32 s18, v252, 13
	v_and_b32_e32 v8, 31, v9
	s_add_u32 s10, s1, s10
	v_or_b32_e32 v166, s18, v8
	s_addc_u32 s11, s4, s11
	v_lshlrev_b64 v[0:1], 7, v[166:167]
	v_and_b32_e32 v2, 0xffffffe0, v9
	v_lshl_add_u64 v[0:1], s[10:11], 0, v[0:1]
	v_ashrrev_i32_e32 v3, 31, v2
	v_lshl_add_u64 v[10:11], v[0:1], 0, v[2:3]
	global_load_dwordx4 v[4:7], v[10:11], off offset:16
	global_load_dwordx4 v[182:185], v[10:11], off
	global_load_dwordx4 v[0:3], v[10:11], off offset:80
	global_load_dwordx4 v[176:179], v[10:11], off offset:64
	v_ashrrev_i32_e32 v48, 3, v9
	s_lshl_b32 s1, s26, 1
	s_ashr_i32 s4, s33, 2
	s_waitcnt vmcnt(1)
	v_add_u32_e32 v2, s84, v48
	s_add_i32 s4, s1, s4
	v_lshrrev_b32_e32 v3, 1, v2
	s_ashr_i32 s5, s4, 31
	v_xor_b32_e32 v3, v3, v9
	s_lshl_b64 s[4:5], s[4:5], 21
	v_lshlrev_b32_e32 v3, 4, v3
	s_add_u32 s14, s80, s4
	v_and_b32_e32 v51, 0x70, v3
	v_lshlrev_b32_e32 v3, 4, v9
	v_mov_b32_e32 v166, v167
	s_addc_u32 s15, s81, s5
	v_and_b32_e32 v6, 0xffffffc0, v3
	v_mov_b32_e32 v163, v160
	v_mov_b32_e32 v164, v161
	v_mov_b32_e32 v165, v162
	v_mov_b64_e32 v[174:175], v[166:167]
	s_mov_b32 m0, s89
	s_add_u32 s16, s82, s4
	v_lshl_or_b32 v2, v2, 7, v51
	v_add_u32_e32 v49, s85, v6
	v_bitop3_b32 v50, v3, 48, v9 bitop3:0x48
	v_mov_b64_e32 v[172:173], v[164:165]
	v_mov_b64_e32 v[170:171], v[162:163]
	v_mov_b64_e32 v[168:169], v[160:161]
	v_mov_b32_e32 v3, v167
	s_addc_u32 s17, s83, s5
	v_or_b32_e32 v6, v49, v50
	v_lshl_add_u64 v[10:11], s[14:15], 0, v[2:3]
	global_load_lds_dwordx4 v2, s[14:15]
	v_mov_b32_e32 v7, v167
	s_add_i32 m0, s89, 0x6000
	v_lshl_add_u64 v[2:3], s[16:17], 0, v[6:7]
	global_load_lds_dwordx4 v6, s[16:17]
	v_lshl_add_u64 v[6:7], v[10:11], 0, s[6:7]
	s_add_i32 m0, s89, 0x2000
	v_lshl_add_u64 v[2:3], v[2:3], 0, s[6:7]
	global_load_lds_dwordx4 v[6:7], off
	v_lshl_add_u64 v[228:229], v[6:7], 0, s[6:7]
	v_readlane_b32 s19, v252, 14
.LBB0_413:
	v_bfe_u32 v3, v9, 1, 3
	v_ashrrev_i32_e32 v7, 4, v9
	v_lshlrev_b32_e32 v6, 7, v8
	v_and_b32_e32 v10, -2, v7
	v_bitop3_b32 v11, v7, v3, -2 bitop3:0x6c
	v_bitop3_b32 v3, v7, v3, 1 bitop3:0x36
	v_lshrrev_b32_e32 v2, 1, v9
	v_lshl_add_u32 v224, v3, 4, v6
	v_add_u32_e32 v3, 4, v10
	v_bitop3_b32 v3, v3, v2, 7 bitop3:0x78
	v_lshl_add_u32 v221, v3, 4, v6
	v_add_u32_e32 v3, 5, v10
	v_bitop3_b32 v2, v3, v2, 7 bitop3:0x78
	v_lshl_add_u32 v222, v2, 4, v6
	v_bfe_u32 v2, v9, 2, 2
	v_lshl_add_u32 v223, v11, 4, v6
	v_lshlrev_b32_e32 v3, 6, v8
	v_bitop3_b32 v6, v7, v2, -2 bitop3:0x6c
	v_bitop3_b32 v2, v7, v2, 1 bitop3:0x36
	v_lshl_add_u32 v220, v2, 4, v3
	s_waitcnt vmcnt(0)
	s_barrier
	v_add_u32_e32 v2, 0, v223
	v_lshl_add_u32 v163, v6, 4, v3
	v_add_u32_e32 v3, 0, v224
	ds_read_b128 v[6:9], v2
	ds_read_b64 v[10:11], v3
	v_mov_b32_e32 v186, v4
	v_mov_b32_e32 v187, v5
	ds_read_b128 v[12:15], v2 offset:4096
	ds_read_b64 v[16:17], v3 offset:4096
	s_waitcnt lgkmcnt(0)
	v_mfma_scale_f32_32x32x64_f8f6f4 v[32:47], v[6:11], v[182:187], 0, v217, v216 op_sel_hi:[0,0,0] cbsz:2 blgp:2
	v_mov_b32_e32 v180, v0
	v_add_u32_e32 v2, 0, v221
	v_add_u32_e32 v3, 0, v222
	ds_read_b128 v[52:55], v2
	ds_read_b64 v[56:57], v3
	v_mov_b32_e32 v181, v1
	ds_read_b128 v[58:61], v2 offset:4096
	ds_read_b64 v[62:63], v3 offset:4096
	s_waitcnt vmcnt(0) lgkmcnt(0)
	v_mfma_scale_f32_32x32x64_f8f6f4 v[32:47], v[52:57], v[176:181], v[32:47], v217, v216 op_sel_hi:[0,0,0] cbsz:2 blgp:2
	s_barrier
	s_mov_b32 m0, s89
	s_cmp_lg_u64 s[60:61], 0
	global_load_lds_dwordx4 v[228:229], off
	s_cbranch_scc1 .Lpro_noconv
	v_mbcnt_lo_u32_b32 v98, -1, 0
	v_mbcnt_hi_u32_b32 v98, -1, v98
	s_mov_b32 m0, s87
	v_ashrrev_i32_e32 v96, 3, v98
	v_mad_i64_i32 v[96:97], s[10:11], s56, v96, 0
	v_lshlrev_b32_e32 v98, 4, v98
	v_lshl_add_u64 v[96:97], v[96:97], 2, s[58:59]
	v_and_b32_e32 v166, 0x70, v98
	v_lshl_add_u64 v[96:97], v[96:97], 0, v[166:167]
	global_load_lds_dwordx4 v[96:97], off nt
.Lpro_noconv:
	s_cmp_lg_u64 s[12:13], 0
	s_cselect_b64 s[54:55], -1, 0
	s_cmp_lt_u32 s0, 2
	s_mov_b32 s0, 0x3f400000
	s_cselect_b64 s[52:53], -1, 0
	s_mov_b32 s8, s9
	v_mfma_scale_f32_32x32x64_f8f6f4 v[16:31], v[12:17], v[182:187], 0, v217, v216 op_sel_hi:[0,0,0] cbsz:2 blgp:2
	s_nop 4
	v_max_f32_e32 v52, v33, v33
	v_max_f32_e32 v53, v32, v32
	v_max_f32_e32 v52, v53, v52
	v_max3_f32 v52, v52, v34, v35
	v_max3_f32 v52, v52, v36, v37
	v_max3_f32 v52, v52, v38, v39
	v_max3_f32 v52, v52, v40, v41
	v_mfma_scale_f32_32x32x64_f8f6f4 v[16:31], v[58:63], v[176:181], v[16:31], v217, v216 op_sel_hi:[0,0,0] cbsz:2 blgp:2
	v_max3_f32 v52, v52, v42, v43
	v_max3_f32 v52, v52, v44, v45
	v_max3_f32 v52, v52, v46, v47
	s_mov_b32 s10, s9
	s_mov_b32 s11, s9
	s_mov_b32 s12, s9
	s_mov_b32 s13, s9
	s_nop 4
	v_max3_f32 v52, v52, v16, v17
	v_max3_f32 v52, v52, v18, v19
	v_max3_f32 v52, v52, v20, v21
	v_max3_f32 v52, v52, v22, v23
	v_max3_f32 v52, v52, v24, v25
	v_max3_f32 v52, v52, v26, v27
	v_max3_f32 v52, v52, v28, v29
	v_max3_f32 v52, v52, v30, v31
	v_mov_b32_e32 v53, v52
	s_nop 1
	v_permlane32_swap_b32_e32 v52, v53
	v_max_f32_e32 v53, v53, v53
	v_max_f32_e32 v52, v52, v52
	v_max_f32_e32 v52, v52, v53
	v_add_f32_e32 v53, 0x7149f2ca, v52
	v_cmp_ge_f32_e32 vcc, s0, v53
	v_max_f32_e32 v52, 0xf149f2ca, v52
	s_cmp_lg_u64 vcc, exec
	v_add_f32_e32 v52, 2.0, v52
	s_cselect_b64 vcc, -1, 0
	v_cndmask_b32_e32 v52, v219, v52, vcc
	v_add_f32_e32 v53, -4.0, v52
	s_lshl_b32 s0, s46, 2
	v_sub_f32_e32 v32, v32, v53
	v_sub_f32_e32 v33, v33, v53
	v_sub_f32_e32 v34, v34, v53
	v_sub_f32_e32 v35, v35, v53
	v_sub_f32_e32 v36, v36, v53
	v_sub_f32_e32 v37, v37, v53
	v_sub_f32_e32 v38, v38, v53
	v_sub_f32_e32 v39, v39, v53
	v_sub_f32_e32 v40, v40, v53
	v_sub_f32_e32 v41, v41, v53
	v_sub_f32_e32 v42, v42, v53
	v_sub_f32_e32 v43, v43, v53
	v_sub_f32_e32 v44, v44, v53
	v_sub_f32_e32 v45, v45, v53
	v_sub_f32_e32 v46, v46, v53
	v_sub_f32_e32 v47, v47, v53
	s_add_i32 s0, s0, 0
	s_mov_b32 s14, s9
	s_mov_b32 s15, s9
	s_mov_b32 s16, s9
	s_mov_b32 s17, s9
	s_mov_b32 s18, s9
	s_mov_b32 s19, s9
	s_mov_b32 s20, s9
	s_mov_b32 s21, s9
	s_mov_b32 s22, s9
	s_mov_b32 s23, s9
	v_mov_b64_e32 v[0:1], s[8:9]
	v_exp_f32_e32 v144, v32
	v_exp_f32_e32 v145, v33
	v_exp_f32_e32 v146, v34
	v_exp_f32_e32 v147, v35
	v_exp_f32_e32 v148, v36
	v_exp_f32_e32 v149, v37
	v_exp_f32_e32 v150, v38
	v_exp_f32_e32 v151, v39
	v_exp_f32_e32 v152, v40
	v_exp_f32_e32 v153, v41
	v_exp_f32_e32 v154, v42
	v_exp_f32_e32 v155, v43
	v_exp_f32_e32 v156, v44
	v_exp_f32_e32 v157, v45
	v_exp_f32_e32 v158, v46
	v_exp_f32_e32 v159, v47
	s_add_i32 s0, s0, 0x1c800
	v_mov_b64_e32 v[2:3], s[10:11]
	v_mov_b64_e32 v[4:5], s[12:13]
	v_mov_b64_e32 v[6:7], s[14:15]
	v_mov_b64_e32 v[8:9], s[16:17]
	v_mov_b64_e32 v[10:11], s[18:19]
	v_mov_b64_e32 v[12:13], s[20:21]
	v_mov_b64_e32 v[14:15], s[22:23]
	v_sub_f32_e32 v128, v16, v53
	s_and_b64 s[10:11], s[52:53], exec
	v_lshlrev_b32_e32 v16, 7, v48
	v_sub_f32_e32 v80, 4.0, v52
	v_sub_f32_e32 v143, v31, v53
	v_sub_f32_e32 v142, v30, v53
	v_sub_f32_e32 v141, v29, v53
	v_sub_f32_e32 v140, v28, v53
	v_sub_f32_e32 v139, v27, v53
	v_sub_f32_e32 v138, v26, v53
	v_sub_f32_e32 v137, v25, v53
	v_sub_f32_e32 v136, v24, v53
	v_sub_f32_e32 v135, v23, v53
	v_sub_f32_e32 v134, v22, v53
	v_sub_f32_e32 v133, v21, v53
	v_sub_f32_e32 v132, v20, v53
	v_sub_f32_e32 v131, v19, v53
	v_sub_f32_e32 v130, v18, v53
	v_sub_f32_e32 v129, v17, v53
	s_cselect_b32 s14, 23, 22
	v_add3_u32 v164, s85, v16, v51
	s_add_u32 s10, s78, s4
	v_add_u32_e32 v174, v49, v50
	v_mov_b64_e32 v[62:63], v[14:15]
	v_mov_b64_e32 v[46:47], v[14:15]
	v_mov_b64_e32 v[30:31], v[14:15]
	v_mov_b64_e32 v[78:79], v[14:15]
	s_mov_b32 s1, 2
	s_mov_b32 s57, 1
	s_mov_b32 s27, -2
	v_mov_b32_e32 v81, v80
	v_mov_b32_e32 v82, v80
	v_mov_b32_e32 v83, v80
	v_mov_b32_e32 v84, v80
	v_mov_b32_e32 v85, v80
	v_mov_b32_e32 v86, v80
	v_mov_b32_e32 v87, v80
	v_mov_b32_e32 v88, v80
	v_mov_b32_e32 v89, v80
	v_mov_b32_e32 v90, v80
	v_mov_b32_e32 v91, v80
	v_mov_b32_e32 v92, v80
	v_mov_b32_e32 v93, v80
	v_mov_b32_e32 v94, v80
	v_mov_b32_e32 v95, v80
	s_mov_b32 s15, 0
	v_mov_b32_e32 v165, v167
	s_addc_u32 s11, s79, s5
	v_mov_b32_e32 v175, v167
	v_mov_b64_e32 v[60:61], v[12:13]
	v_mov_b64_e32 v[58:59], v[10:11]
	v_mov_b64_e32 v[56:57], v[8:9]
	v_mov_b64_e32 v[54:55], v[6:7]
	v_mov_b64_e32 v[52:53], v[4:5]
	v_mov_b64_e32 v[50:51], v[2:3]
	v_mov_b64_e32 v[48:49], v[0:1]
	v_mov_b64_e32 v[44:45], v[12:13]
	v_mov_b64_e32 v[42:43], v[10:11]
	v_mov_b64_e32 v[40:41], v[8:9]
	v_mov_b64_e32 v[38:39], v[6:7]
	v_mov_b64_e32 v[36:37], v[4:5]
	v_mov_b64_e32 v[34:35], v[2:3]
	v_mov_b64_e32 v[32:33], v[0:1]
	v_mov_b64_e32 v[28:29], v[12:13]
	v_mov_b64_e32 v[26:27], v[10:11]
	v_mov_b64_e32 v[24:25], v[8:9]
	v_mov_b64_e32 v[22:23], v[6:7]
	v_mov_b64_e32 v[20:21], v[4:5]
	v_mov_b64_e32 v[18:19], v[2:3]
	v_mov_b64_e32 v[16:17], v[0:1]
	s_mov_b32 s16, 2
	v_mov_b64_e32 v[76:77], v[12:13]
	v_mov_b64_e32 v[74:75], v[10:11]
	v_mov_b64_e32 v[72:73], v[8:9]
	v_mov_b64_e32 v[70:71], v[6:7]
	v_mov_b64_e32 v[68:69], v[4:5]
	v_mov_b64_e32 v[66:67], v[2:3]
	v_mov_b64_e32 v[64:65], v[0:1]
	v_mbcnt_lo_u32_b32 v200, -1, 0
	v_mbcnt_hi_u32_b32 v200, -1, v200
	v_lshrrev_b32_e32 v201, 3, v200
	v_mul_lo_u32 v201, v201, s56
	v_and_b32_e32 v200, 7, v200
	v_lshl_or_b32 v214, v201, 2, v200
	ds_read_b128 v[228:231], v223 offset:8192
	ds_read_b64 v[232:233], v224 offset:8192
	ds_read_b128 v[234:237], v223 offset:12288
	ds_read_b64 v[238:239], v224 offset:12288
	ds_read_b128 v[240:243], v221 offset:8192
	ds_read_b64 v[244:245], v222 offset:8192
	ds_read_b128 v[246:249], v221 offset:12288
	ds_read_b64 v[250:251], v222 offset:12288

.LBB0_417:
	s_add_u32 s12, s10, 0x74006000
	s_addc_u32 s13, s11, 0
	s_barrier
	s_add_i32 m0, s89, 0x2000
	s_add_u32 s4, s10, 0x74802000
	global_load_lds_dwordx4 v164, s[12:13]
	s_addc_u32 s5, s11, 0
	s_add_i32 m0, s89, 0x8000
	s_andn2_b64 vcc, exec, s[62:63]
	global_load_lds_dwordx4 v174, s[4:5]
	s_cbranch_vccnz .LBB0_419
	s_add_i32 s8, s1, -1
	s_and_b32 s17, s8, 7
	s_lshr_b32 s8, s8, 3
	s_lshl_b64 s[12:13], s[8:9], 24
	s_add_u32 s12, s58, s12
	s_addc_u32 s13, s59, s13
	s_mul_i32 s4, s17, s56
	s_lshl_b32 s4, s4, 5
	s_add_u32 s12, s12, s4
	s_addc_u32 s13, s13, 0
	s_add_i32 s4, s27, 1
	v_add_lshl_u32 v96, v214, s4, 4
	v_and_b32_e32 v96, 0x70, v96
	v_and_or_b32 v96, v214, -8, v96
	s_lshl_b32 s4, s17, 10
	s_add_i32 s4, s66, s4
	s_add_i32 m0, s4, 0xc800
	s_nop 0
	global_load_lds_dwordx4 v96, s[12:13] nt
.LBB0_419:
	v_mfma_scale_f32_32x32x64_f8f6f4 v[112:127], v[228:233], v[182:187], v[80:95], v217, v216 op_sel_hi:[0,0,0] cbsz:2 blgp:2
	v_exp_f32_e32 v128, v128
	v_exp_f32_e32 v129, v129
	v_exp_f32_e32 v130, v130
	v_exp_f32_e32 v131, v131
	v_mfma_scale_f32_32x32x64_f8f6f4 v[96:111], v[234:239], v[182:187], v[80:95], v217, v216 op_sel_hi:[0,0,0] cbsz:2 blgp:2
	v_exp_f32_e32 v132, v132
	v_exp_f32_e32 v133, v133
	v_exp_f32_e32 v134, v134
	v_exp_f32_e32 v135, v135
	v_mfma_scale_f32_32x32x64_f8f6f4 v[112:127], v[240:245], v[176:181], v[112:127], v217, v216 op_sel_hi:[0,0,0] cbsz:2 blgp:2
	v_exp_f32_e32 v136, v136
	v_exp_f32_e32 v137, v137
	v_exp_f32_e32 v138, v138
	v_exp_f32_e32 v139, v139
	v_mfma_scale_f32_32x32x64_f8f6f4 v[96:111], v[246:251], v[176:181], v[96:111], v217, v216 op_sel_hi:[0,0,0] cbsz:2 blgp:2
	ds_read_b128 v[228:231], v223
	ds_read_b64 v[232:233], v224
	ds_read_b128 v[234:237], v223 offset:4096
	ds_read_b64 v[238:239], v224 offset:4096
	ds_read_b128 v[240:243], v221
	ds_read_b64 v[244:245], v222
	ds_read_b128 v[246:249], v221 offset:4096
	ds_read_b64 v[250:251], v222 offset:4096
	ds_read_b128 v[206:209], v163 offset:24576
	ds_read_b64 v[210:211], v220 offset:24576
	ds_read_b128 v[200:203], v163 offset:26624
	ds_read_b64 v[204:205], v220 offset:26624
	ds_read_b128 v[194:197], v163 offset:28672
	ds_read_b64 v[198:199], v220 offset:28672
	ds_read_b128 v[188:191], v163 offset:30720
	ds_read_b64 v[192:193], v220 offset:30720
	v_exp_f32_e32 v140, v140
	v_exp_f32_e32 v141, v141
	v_exp_f32_e32 v142, v142
	v_exp_f32_e32 v143, v143
	s_nop 0
	v_cvt_scalef32_2xpk16_bf6_f32 v[128:133], v[144:159], v[128:143], 1.0
	s_nop 1
	v_mfma_scale_f32_32x32x64_f8f6f4 v[64:79], v[128:133], v[168:173], v[64:79], v218, v218 op_sel_hi:[0,0,0] cbsz:3 blgp:2
	v_max_f32_e32 v225, v113, v113
	v_max_f32_e32 v226, v112, v112
	v_max_f32_e32 v225, v226, v225
	v_max3_f32 v225, v225, v114, v115
	s_waitcnt lgkmcnt(0)
	v_mfma_scale_f32_32x32x64_f8f6f4 v[0:15], v[128:133], v[206:211], v[0:15], v218, v217 op_sel_hi:[0,0,0] cbsz:3 blgp:2
	v_max3_f32 v225, v225, v116, v117
	v_max3_f32 v225, v225, v118, v119
	v_max3_f32 v225, v225, v120, v121
	v_max3_f32 v225, v225, v122, v123
	v_mfma_scale_f32_32x32x64_f8f6f4 v[48:63], v[128:133], v[200:205], v[48:63], v218, v217 op_sel_hi:[0,0,0] cbsz:3 blgp:2
	v_max3_f32 v225, v225, v124, v125
	v_max3_f32 v225, v225, v126, v127
	v_max3_f32 v225, v225, v96, v97
	v_max3_f32 v225, v225, v98, v99
	v_mfma_scale_f32_32x32x64_f8f6f4 v[32:47], v[128:133], v[194:199], v[32:47], v218, v217 op_sel_hi:[0,0,0] cbsz:3 blgp:2
	v_max3_f32 v225, v225, v100, v101
	v_max3_f32 v225, v225, v102, v103
	v_max3_f32 v225, v225, v104, v105
	v_max3_f32 v225, v225, v106, v107
	v_mfma_scale_f32_32x32x64_f8f6f4 v[16:31], v[128:133], v[188:193], v[16:31], v218, v217 op_sel_hi:[0,0,0] cbsz:3 blgp:2
	v_max3_f32 v225, v225, v108, v109
	v_max3_f32 v225, v225, v110, v111
	v_cmp_nge_f32_e32 vcc, s2, v225
	s_cbranch_vccnz .LBB0_444

.LBB0_428:
	s_add_u32 s12, s10, 0x74008000
	s_addc_u32 s13, s11, 0
	s_barrier
	s_mov_b32 m0, s89
	s_add_u32 s4, s10, 0x74804000
	global_load_lds_dwordx4 v164, s[12:13]
	s_addc_u32 s5, s11, 0
	s_add_i32 m0, s89, 0x6000
	s_and_b64 vcc, exec, s[60:61]
	global_load_lds_dwordx4 v174, s[4:5]
	s_cbranch_vccnz .LBB0_437
	s_and_b32 s17, s1, 7
	s_cmp_eq_u32 s17, 0
	s_cbranch_scc1 .LBB0_431
	s_lshr_b32 s8, s1, 3
	s_cbranch_execz .LBB0_432
	s_branch .LBB0_436

.LBB0_437:
	v_mfma_scale_f32_32x32x64_f8f6f4 v[144:159], v[228:233], v[182:187], v[80:95], v217, v216 op_sel_hi:[0,0,0] cbsz:2 blgp:2
	v_exp_f32_e32 v96, v96
	v_exp_f32_e32 v97, v97
	v_exp_f32_e32 v98, v98
	v_exp_f32_e32 v99, v99
	v_mfma_scale_f32_32x32x64_f8f6f4 v[128:143], v[234:239], v[182:187], v[80:95], v217, v216 op_sel_hi:[0,0,0] cbsz:2 blgp:2
	v_exp_f32_e32 v100, v100
	v_exp_f32_e32 v101, v101
	v_exp_f32_e32 v102, v102
	v_exp_f32_e32 v103, v103
	v_mfma_scale_f32_32x32x64_f8f6f4 v[144:159], v[240:245], v[176:181], v[144:159], v217, v216 op_sel_hi:[0,0,0] cbsz:2 blgp:2
	v_exp_f32_e32 v104, v104
	v_exp_f32_e32 v105, v105
	v_exp_f32_e32 v106, v106
	v_exp_f32_e32 v107, v107
	v_mfma_scale_f32_32x32x64_f8f6f4 v[128:143], v[246:251], v[176:181], v[128:143], v217, v216 op_sel_hi:[0,0,0] cbsz:2 blgp:2
	ds_read_b128 v[228:231], v223 offset:8192
	ds_read_b64 v[232:233], v224 offset:8192
	ds_read_b128 v[234:237], v223 offset:12288
	ds_read_b64 v[238:239], v224 offset:12288
	ds_read_b128 v[240:243], v221 offset:8192
	ds_read_b64 v[244:245], v222 offset:8192
	ds_read_b128 v[246:249], v221 offset:12288
	ds_read_b64 v[250:251], v222 offset:12288
	ds_read_b128 v[206:209], v163 offset:32768
	ds_read_b64 v[210:211], v220 offset:32768
	ds_read_b128 v[200:203], v163 offset:34816
	ds_read_b64 v[204:205], v220 offset:34816
	ds_read_b128 v[194:197], v163 offset:36864
	ds_read_b64 v[198:199], v220 offset:36864
	ds_read_b128 v[188:191], v163 offset:38912
	ds_read_b64 v[192:193], v220 offset:38912
	v_exp_f32_e32 v108, v108
	v_exp_f32_e32 v109, v109
	v_exp_f32_e32 v110, v110
	v_exp_f32_e32 v111, v111
	s_nop 0
	v_cvt_scalef32_2xpk16_bf6_f32 v[96:101], v[112:127], v[96:111], 1.0
	s_nop 1
	v_mfma_scale_f32_32x32x64_f8f6f4 v[64:79], v[96:101], v[168:173], v[64:79], v218, v218 op_sel_hi:[0,0,0] cbsz:3 blgp:2
	v_max_f32_e32 v212, v145, v145
	v_max_f32_e32 v213, v144, v144
	v_max_f32_e32 v212, v213, v212
	v_max3_f32 v212, v212, v146, v147
	s_waitcnt lgkmcnt(0)
	v_mfma_scale_f32_32x32x64_f8f6f4 v[0:15], v[96:101], v[206:211], v[0:15], v218, v217 op_sel_hi:[0,0,0] cbsz:3 blgp:2
	v_max3_f32 v212, v212, v148, v149
	v_max3_f32 v212, v212, v150, v151
	v_max3_f32 v212, v212, v152, v153
	v_max3_f32 v212, v212, v154, v155
	v_mfma_scale_f32_32x32x64_f8f6f4 v[48:63], v[96:101], v[200:205], v[48:63], v218, v217 op_sel_hi:[0,0,0] cbsz:3 blgp:2
	v_max3_f32 v212, v212, v156, v157
	v_max3_f32 v212, v212, v158, v159
	v_max3_f32 v212, v212, v128, v129
	v_max3_f32 v212, v212, v130, v131
	v_mfma_scale_f32_32x32x64_f8f6f4 v[32:47], v[96:101], v[194:199], v[32:47], v218, v217 op_sel_hi:[0,0,0] cbsz:3 blgp:2
	v_max3_f32 v212, v212, v132, v133
	v_max3_f32 v212, v212, v134, v135
	v_max3_f32 v212, v212, v136, v137
	v_max3_f32 v212, v212, v138, v139
	v_mfma_scale_f32_32x32x64_f8f6f4 v[16:31], v[96:101], v[188:193], v[16:31], v218, v217 op_sel_hi:[0,0,0] cbsz:3 blgp:2
	v_max3_f32 v212, v212, v140, v141
	v_max3_f32 v212, v212, v142, v143
	v_cmp_nge_f32_e32 vcc, s2, v212
	s_cbranch_vccnz .LBB0_445
.LBB0_442:
	v_exp_f32_e32 v144, v144
	v_exp_f32_e32 v145, v145
	v_exp_f32_e32 v146, v146
	v_exp_f32_e32 v147, v147
	v_exp_f32_e32 v148, v148
	v_exp_f32_e32 v149, v149
	v_exp_f32_e32 v150, v150
	v_exp_f32_e32 v151, v151
	v_exp_f32_e32 v152, v152
	v_exp_f32_e32 v153, v153
	v_exp_f32_e32 v154, v154
	v_exp_f32_e32 v155, v155
	v_exp_f32_e32 v156, v156
	v_exp_f32_e32 v157, v157
	v_exp_f32_e32 v158, v158
	v_exp_f32_e32 v159, v159
	s_add_i32 s27, s27, -2
	s_add_u32 s10, s10, 0x4000
	s_addc_u32 s11, s11, 0
	s_add_i32 s1, s1, 2
	s_cmpk_gt_u32 s1, 0xff
	s_cbranch_scc0 .Lattn_top
	s_branch .LBB0_446

.LBB0_438:
	v_cmp_gt_f32_e32 vcc, 1.0, v166
	s_cbranch_vccz .LBB0_442
	v_mbcnt_lo_u32_b32 v96, -1, 0
	v_mbcnt_hi_u32_b32 v96, -1, v96
	s_nop 0
	v_cmp_gt_u32_e32 vcc, 32, v96
	s_and_saveexec_b64 s[12:13], vcc
	v_lshl_add_u32 v97, v96, 2, s86
	ds_write_b32 v97, v166 offset:49152
	s_or_b64 exec, exec, s[12:13]
	v_ashrrev_i32_e32 v96, 3, v96
	v_lshlrev_b32_e32 v96, 2, v96
	v_and_b32_e32 v96, -16, v96
	s_waitcnt lgkmcnt(0)
	v_add_u32_e32 v108, s86, v96
	ds_read_b128 v[96:99], v108 offset:49248
	ds_read_b128 v[100:103], v108 offset:49216
	ds_read_b128 v[104:107], v108 offset:49184
	ds_read_b128 v[108:111], v108 offset:49152
	s_waitcnt lgkmcnt(0)
	v_pk_mul_f32 v[12:13], v[12:13], v[96:97]
	v_pk_mul_f32 v[8:9], v[8:9], v[100:101]
	v_pk_mul_f32 v[4:5], v[4:5], v[104:105]
	v_pk_mul_f32 v[14:15], v[14:15], v[98:99]
	v_pk_mul_f32 v[10:11], v[10:11], v[102:103]
	v_pk_mul_f32 v[6:7], v[6:7], v[106:107]
	v_pk_mul_f32 v[2:3], v[2:3], v[110:111]
	v_pk_mul_f32 v[0:1], v[0:1], v[108:109]
	v_pk_mul_f32 v[60:61], v[60:61], v[96:97]
	v_pk_mul_f32 v[56:57], v[56:57], v[100:101]
	v_pk_mul_f32 v[52:53], v[52:53], v[104:105]
	v_pk_mul_f32 v[62:63], v[62:63], v[98:99]
	v_pk_mul_f32 v[58:59], v[58:59], v[102:103]
	v_pk_mul_f32 v[54:55], v[54:55], v[106:107]
	v_pk_mul_f32 v[50:51], v[50:51], v[110:111]
	v_pk_mul_f32 v[48:49], v[48:49], v[108:109]
	v_pk_mul_f32 v[44:45], v[44:45], v[96:97]
	v_pk_mul_f32 v[40:41], v[40:41], v[100:101]
	v_pk_mul_f32 v[36:37], v[36:37], v[104:105]
	v_pk_mul_f32 v[46:47], v[46:47], v[98:99]
	v_pk_mul_f32 v[42:43], v[42:43], v[102:103]
	v_pk_mul_f32 v[38:39], v[38:39], v[106:107]
	v_pk_mul_f32 v[34:35], v[34:35], v[110:111]
	v_pk_mul_f32 v[32:33], v[32:33], v[108:109]
	v_pk_mul_f32 v[28:29], v[28:29], v[96:97]
	v_pk_mul_f32 v[24:25], v[24:25], v[100:101]
	v_pk_mul_f32 v[20:21], v[20:21], v[104:105]
	v_pk_mul_f32 v[30:31], v[30:31], v[98:99]
	v_pk_mul_f32 v[26:27], v[26:27], v[102:103]
	v_pk_mul_f32 v[22:23], v[22:23], v[106:107]
	v_pk_mul_f32 v[18:19], v[18:19], v[110:111]
	v_pk_mul_f32 v[16:17], v[16:17], v[108:109]
	v_pk_mul_f32 v[76:77], v[76:77], v[96:97]
	v_pk_mul_f32 v[72:73], v[72:73], v[100:101]
	v_pk_mul_f32 v[68:69], v[68:69], v[104:105]
	v_pk_mul_f32 v[78:79], v[78:79], v[98:99]
	v_pk_mul_f32 v[74:75], v[74:75], v[102:103]
	v_pk_mul_f32 v[70:71], v[70:71], v[106:107]
	v_pk_mul_f32 v[66:67], v[66:67], v[110:111]
	v_pk_mul_f32 v[64:65], v[64:65], v[108:109]
	s_branch .LBB0_442
.Lep_w0:
	s_waitcnt vmcnt(0) lgkmcnt(0)
	s_branch .LBB0_450
.LBB0_446:
	s_cmp_lg_u64 s[60:61], 0
	s_cbranch_scc1 .Lep_w0
	s_waitcnt vmcnt(1) lgkmcnt(0)
.LBB0_450:
	s_barrier
	s_add_u32 s4, s10, 0x74802000
	s_addc_u32 s5, s11, 0
	s_add_i32 m0, s89, 0x8000
	s_nop 0
	global_load_lds_dwordx4 v174, s[4:5]
	s_and_b64 vcc, exec, s[60:61]
	s_cbranch_vccnz .LBB0_452
	v_mbcnt_lo_u32_b32 v98, -1, 0
	v_mbcnt_hi_u32_b32 v98, -1, v98
	s_mov_b32 m0, s88
	v_ashrrev_i32_e32 v96, 3, v98
	v_add_u32_e32 v96, 56, v96
	v_lshl_add_u32 v98, v98, 2, 4
	v_mad_i64_i32 v[96:97], s[10:11], s56, v96, 0
	v_and_b32_e32 v98, 28, v98
	v_lshl_add_u64 v[96:97], v[96:97], 2, s[58:59]
	v_lshlrev_b32_e32 v166, 2, v98
	v_lshl_add_u64 v[96:97], v[96:97], 0, v[166:167]
	s_mov_b64 s[10:11], 0x1f000000
	v_lshl_add_u64 v[96:97], v[96:97], 0, s[10:11]
	global_load_lds_dwordx4 v[96:97], off nt
.LBB0_452:
	v_mov_b32_e32 v164, 1.0
	s_waitcnt lgkmcnt(0)
	v_mfma_scale_f32_32x32x64_f8f6f4 v[96:111], v[228:233], v[182:187], v[80:95], v217, v216 op_sel_hi:[0,0,0] cbsz:2 blgp:2
	v_mfma_scale_f32_32x32x64_f8f6f4 v[80:95], v[234:239], v[182:187], v[80:95], v217, v216 op_sel_hi:[0,0,0] cbsz:2 blgp:2
	v_mfma_scale_f32_32x32x64_f8f6f4 v[96:111], v[240:245], v[176:181], v[96:111], v217, v216 op_sel_hi:[0,0,0] cbsz:2 blgp:2
	v_mfma_scale_f32_32x32x64_f8f6f4 v[80:95], v[246:251], v[176:181], v[80:95], v217, v216 op_sel_hi:[0,0,0] cbsz:2 blgp:2
	s_mov_b32 s1, 0
	s_add_i32 s8, s1, 0
	v_add_u32_e32 v112, s8, v163
	v_add_u32_e32 v113, s8, v220
	ds_read_b128 v[192:195], v112 offset:24576
	ds_read_b64 v[196:197], v113 offset:24576
	ds_read_b128 v[186:189], v112 offset:26624
	ds_read_b64 v[190:191], v113 offset:26624
	ds_read_b128 v[180:183], v112 offset:28672
	ds_read_b64 v[184:185], v113 offset:28672
	ds_read_b128 v[174:177], v112 offset:30720
	ds_read_b64 v[178:179], v113 offset:30720
	v_max_f32_e32 v112, v97, v97
	v_max_f32_e32 v113, v96, v96
	v_max_f32_e32 v112, v113, v112
	v_max3_f32 v112, v112, v98, v99
	v_max3_f32 v112, v112, v100, v101
	v_max3_f32 v112, v112, v102, v103
	v_max3_f32 v112, v112, v104, v105
	v_max3_f32 v112, v112, v106, v107
	v_max3_f32 v112, v112, v108, v109
	v_max3_f32 v112, v112, v110, v111
	v_max3_f32 v112, v112, v80, v81
	v_max3_f32 v112, v112, v82, v83
	v_max3_f32 v112, v112, v84, v85
	v_max3_f32 v112, v112, v86, v87
	v_max3_f32 v112, v112, v88, v89
	v_max3_f32 v112, v112, v90, v91
	v_max3_f32 v112, v112, v92, v93
	v_max3_f32 v112, v112, v94, v95
	v_mov_b32_e32 v113, v112
	s_nop 1
	v_permlane32_swap_b32_e32 v112, v113
	v_max_f32_e32 v113, v113, v113
	v_max_f32_e32 v112, v112, v112
	v_max_f32_e32 v112, v112, v113
	v_cmp_ge_f32_e32 vcc, s2, v112
	s_cmp_eq_u64 vcc, exec
	s_cbranch_scc0 .LBB0_460

.LBB0_457:
	s_waitcnt vmcnt(0)
	s_barrier
	s_mov_b32 s1, 0x2000
	s_add_i32 s1, s1, 0
	v_add_u32_e32 v112, s1, v163
	v_add_u32_e32 v116, s1, v220
	ds_read_b128 v[130:133], v112 offset:24576
	ds_read_b64 v[134:135], v116 offset:24576
	ds_read_b128 v[124:127], v112 offset:26624
	ds_read_b64 v[128:129], v116 offset:26624
	ds_read_b128 v[118:121], v112 offset:28672
	ds_read_b64 v[122:123], v116 offset:28672
	ds_read_b128 v[112:115], v112 offset:30720
	ds_read_b64 v[116:117], v116 offset:30720
	s_and_b64 vcc, exec, s[60:61]
	s_cbranch_vccnz .LBB0_377
	s_waitcnt vmcnt(0)
	v_mbcnt_lo_u32_b32 v145, -1, 0
	v_mbcnt_hi_u32_b32 v145, -1, v145
	s_andn2_b64 vcc, exec, s[54:55]
	v_and_b32_e32 v144, 7, v145
	s_cbranch_vccz .LBB0_375
	v_mov_b32_e32 v138, 0x42800000
	v_mov_b32_e32 v139, 0x42800000
	v_mov_b32_e32 v136, 0x42800000
	v_mov_b32_e32 v137, 0x42800000
	v_mov_b32_e32 v142, 0x42800000
	v_mov_b32_e32 v143, 0x42800000
	v_mov_b32_e32 v140, 0x42800000
	v_mov_b32_e32 v141, 0x42800000
	s_branch .LBB0_376
